# layer-1 out-proj residual epilogue: 32 bf16 residual loads in flight (was 4 at a time); R2/M2 hand-written chains back in
# speedup vs baseline: 1.0062x; 1.0062x over previous
; DI unsigned pkbf(float lo, float hi) { typedef __bf16 b2 __attribute__((ext_vector_type(2))); typedef float f2 __attribute__((ext_vector_type(2))); const f2 v = {lo, hi}; return __builtin_bit_cast(unsigned, __builtin_convertvector(v, b2)); }
;     DI void operator()(const pg8::f32x4 (&acc)[2][2][4][2], const pg8::Unit& u, int wr, int wc, int fr, int fq) const {
;         const int row0 = u.pm * 256 + wr * 64 + fr, col0 = u.pn * 256 + wc * 32 + 4 * fq;
; #pragma unroll
;         for (int ai = 0; ai < 2; ++ai)
; #pragma unroll
;             for (int m = 0; m < 4; ++m) { const size_t off = (size_t)(row0 + ai * 128 + m * 16) * ldc + col0;
; #pragma unroll
;                 for (int bj = 0; bj < 2; ++bj)
; #pragma unroll
;                     for (int n = 0; n < 2; ++n) { pg8::f32x4 b;
;                         if constexpr (BASE_BF16) { const uint2 w = *(const uint2*)((const bf16*)base + off + bj * 128 + n * 16);
;                             b[0] = __uint_as_float(w.x << 16); b[1] = __uint_as_float(w.x & 0xffff0000u); b[2] = __uint_as_float(w.y << 16); b[3] = __uint_as_float(w.y & 0xffff0000u); }
;                         else b = *(const pg8::f32x4*)((const float*)base + off + bj * 128 + n * 16);
;                         b += acc[ai][bj][m][n]; uint2 o; o.x = pkbf(b[0], b[1]); o.y = pkbf(b[2], b[3]); *(uint2*)(out + off + bj * 128 + n * 16) = o; } }
.LBB0_2573:
	v_lshl_add_u32 v148, s30, 8, v1
	v_lshl_or_b32 v144, s55, 8, v151
	v_ashrrev_i32_e32 v149, 31, v148
	v_ashrrev_i32_e32 v145, 31, v144
	v_lshlrev_b64 v[142:143], 10, v[148:149]
	v_lshl_add_u64 v[142:143], v[142:143], 0, v[144:145]
	v_lshlrev_b64 v[142:143], 1, v[142:143]
	v_lshl_add_u64 v[156:157], s[8:9], 0, v[142:143]
	v_lshl_add_u64 v[166:167], s[10:11], 0, v[142:143]
	s_mov_b64 s[34:35], 0x8000
	s_mov_b64 s[36:37], 0x28000
	global_load_dwordx2 v[172:173], v[156:157], off
	global_load_dwordx2 v[174:175], v[156:157], off offset:32
	global_load_dwordx2 v[176:177], v[156:157], off offset:256
	global_load_dwordx2 v[178:179], v[156:157], off offset:288
	v_lshl_add_u64 v[156:157], v[156:157], 0, s[34:35]
	global_load_dwordx2 v[180:181], v[156:157], off
	global_load_dwordx2 v[182:183], v[156:157], off offset:32
	global_load_dwordx2 v[184:185], v[156:157], off offset:256
	global_load_dwordx2 v[186:187], v[156:157], off offset:288
	v_lshl_add_u64 v[156:157], v[156:157], 0, s[34:35]
	global_load_dwordx2 v[188:189], v[156:157], off
	global_load_dwordx2 v[190:191], v[156:157], off offset:32
	global_load_dwordx2 v[192:193], v[156:157], off offset:256
	global_load_dwordx2 v[194:195], v[156:157], off offset:288
	v_lshl_add_u64 v[156:157], v[156:157], 0, s[34:35]
	global_load_dwordx2 v[196:197], v[156:157], off
	global_load_dwordx2 v[198:199], v[156:157], off offset:32
	global_load_dwordx2 v[200:201], v[156:157], off offset:256
	global_load_dwordx2 v[202:203], v[156:157], off offset:288
	v_lshl_add_u64 v[156:157], v[156:157], 0, s[36:37]
	global_load_dwordx2 v[204:205], v[156:157], off
	global_load_dwordx2 v[206:207], v[156:157], off offset:32
	global_load_dwordx2 v[208:209], v[156:157], off offset:256
	global_load_dwordx2 v[210:211], v[156:157], off offset:288
	v_lshl_add_u64 v[156:157], v[156:157], 0, s[34:35]
	global_load_dwordx2 v[212:213], v[156:157], off
	global_load_dwordx2 v[214:215], v[156:157], off offset:32
	global_load_dwordx2 v[216:217], v[156:157], off offset:256
	global_load_dwordx2 v[218:219], v[156:157], off offset:288
	v_lshl_add_u64 v[156:157], v[156:157], 0, s[34:35]
	global_load_dwordx2 v[220:221], v[156:157], off
	global_load_dwordx2 v[222:223], v[156:157], off offset:32
	global_load_dwordx2 v[224:225], v[156:157], off offset:256
	global_load_dwordx2 v[226:227], v[156:157], off offset:288
	v_lshl_add_u64 v[156:157], v[156:157], 0, s[34:35]
	global_load_dwordx2 v[228:229], v[156:157], off
	global_load_dwordx2 v[230:231], v[156:157], off offset:32
	global_load_dwordx2 v[236:237], v[156:157], off offset:256
	global_load_dwordx2 v[238:239], v[156:157], off offset:288
	s_waitcnt vmcnt(31)
	v_lshlrev_b32_e32 v158, 16, v172
	v_and_b32_e32 v159, 0xffff0000, v172
	v_lshlrev_b32_e32 v160, 16, v173
	v_and_b32_e32 v161, 0xffff0000, v173
	v_pk_add_f32 v[126:127], v[126:127], v[158:159]
	v_pk_add_f32 v[128:129], v[128:129], v[160:161]
	v_cvt_pk_bf16_f32 v126, v126, v127
	v_cvt_pk_bf16_f32 v127, v128, v129
	global_store_dwordx2 v[166:167], v[126:127], off
	s_waitcnt vmcnt(31)
	v_lshlrev_b32_e32 v162, 16, v174
	v_and_b32_e32 v163, 0xffff0000, v174
	v_lshlrev_b32_e32 v164, 16, v175
	v_and_b32_e32 v165, 0xffff0000, v175
	v_pk_add_f32 v[122:123], v[122:123], v[162:163]
	v_pk_add_f32 v[124:125], v[124:125], v[164:165]
	v_cvt_pk_bf16_f32 v122, v122, v123
	v_cvt_pk_bf16_f32 v123, v124, v125
	global_store_dwordx2 v[166:167], v[122:123], off offset:32
	s_waitcnt vmcnt(31)
	v_lshlrev_b32_e32 v158, 16, v176
	v_and_b32_e32 v159, 0xffff0000, v176
	v_lshlrev_b32_e32 v160, 16, v177
	v_and_b32_e32 v161, 0xffff0000, v177
	v_pk_add_f32 v[118:119], v[118:119], v[158:159]
	v_pk_add_f32 v[120:121], v[120:121], v[160:161]
	v_cvt_pk_bf16_f32 v118, v118, v119
	v_cvt_pk_bf16_f32 v119, v120, v121
	global_store_dwordx2 v[166:167], v[118:119], off offset:256
	s_waitcnt vmcnt(31)
	v_lshlrev_b32_e32 v162, 16, v178
	v_and_b32_e32 v163, 0xffff0000, v178
	v_lshlrev_b32_e32 v164, 16, v179
	v_and_b32_e32 v165, 0xffff0000, v179
	v_pk_add_f32 v[114:115], v[114:115], v[162:163]
	v_pk_add_f32 v[116:117], v[116:117], v[164:165]
	v_cvt_pk_bf16_f32 v114, v114, v115
	v_cvt_pk_bf16_f32 v115, v116, v117
	global_store_dwordx2 v[166:167], v[114:115], off offset:288
	v_lshl_add_u64 v[166:167], v[166:167], 0, s[34:35]
	s_waitcnt vmcnt(31)
	v_lshlrev_b32_e32 v158, 16, v180
	v_and_b32_e32 v159, 0xffff0000, v180
	v_lshlrev_b32_e32 v160, 16, v181
	v_and_b32_e32 v161, 0xffff0000, v181
	v_pk_add_f32 v[110:111], v[110:111], v[158:159]
	v_pk_add_f32 v[112:113], v[112:113], v[160:161]
	v_cvt_pk_bf16_f32 v110, v110, v111
	v_cvt_pk_bf16_f32 v111, v112, v113
	global_store_dwordx2 v[166:167], v[110:111], off
	s_waitcnt vmcnt(31)
	v_lshlrev_b32_e32 v162, 16, v182
	v_and_b32_e32 v163, 0xffff0000, v182
	v_lshlrev_b32_e32 v164, 16, v183
	v_and_b32_e32 v165, 0xffff0000, v183
	v_pk_add_f32 v[106:107], v[106:107], v[162:163]
	v_pk_add_f32 v[108:109], v[108:109], v[164:165]
	v_cvt_pk_bf16_f32 v106, v106, v107
	v_cvt_pk_bf16_f32 v107, v108, v109
	global_store_dwordx2 v[166:167], v[106:107], off offset:32
	s_waitcnt vmcnt(31)
	v_lshlrev_b32_e32 v158, 16, v184
	v_and_b32_e32 v159, 0xffff0000, v184
	v_lshlrev_b32_e32 v160, 16, v185
	v_and_b32_e32 v161, 0xffff0000, v185
	v_pk_add_f32 v[102:103], v[102:103], v[158:159]
	v_pk_add_f32 v[104:105], v[104:105], v[160:161]
	v_cvt_pk_bf16_f32 v102, v102, v103
	v_cvt_pk_bf16_f32 v103, v104, v105
	global_store_dwordx2 v[166:167], v[102:103], off offset:256
	s_waitcnt vmcnt(31)
; DI unsigned pkbf(float lo, float hi) { typedef __bf16 b2 __attribute__((ext_vector_type(2))); typedef float f2 __attribute__((ext_vector_type(2))); const f2 v = {lo, hi}; return __builtin_bit_cast(unsigned, __builtin_convertvector(v, b2)); }
;     DI void operator()(const pg8::f32x4 (&acc)[2][2][4][2], const pg8::Unit& u, int wr, int wc, int fr, int fq) const {
;         const int row0 = u.pm * 256 + wr * 64 + fr, col0 = u.pn * 256 + wc * 32 + 4 * fq;
; #pragma unroll
;         for (int ai = 0; ai < 2; ++ai)
; #pragma unroll
;             for (int m = 0; m < 4; ++m) { const size_t off = (size_t)(row0 + ai * 128 + m * 16) * ldc + col0;
; #pragma unroll
;                 for (int bj = 0; bj < 2; ++bj)
; #pragma unroll
;                     for (int n = 0; n < 2; ++n) { pg8::f32x4 b;
;                         if constexpr (BASE_BF16) { const uint2 w = *(const uint2*)((const bf16*)base + off + bj * 128 + n * 16);
;                             b[0] = __uint_as_float(w.x << 16); b[1] = __uint_as_float(w.x & 0xffff0000u); b[2] = __uint_as_float(w.y << 16); b[3] = __uint_as_float(w.y & 0xffff0000u); }
;                         else b = *(const pg8::f32x4*)((const float*)base + off + bj * 128 + n * 16);
;                         b += acc[ai][bj][m][n]; uint2 o; o.x = pkbf(b[0], b[1]); o.y = pkbf(b[2], b[3]); *(uint2*)(out + off + bj * 128 + n * 16) = o; } }
	v_lshlrev_b32_e32 v162, 16, v186
	v_and_b32_e32 v163, 0xffff0000, v186
	v_lshlrev_b32_e32 v164, 16, v187
	v_and_b32_e32 v165, 0xffff0000, v187
	v_pk_add_f32 v[98:99], v[98:99], v[162:163]
	v_pk_add_f32 v[100:101], v[100:101], v[164:165]
	v_cvt_pk_bf16_f32 v98, v98, v99
	v_cvt_pk_bf16_f32 v99, v100, v101
	global_store_dwordx2 v[166:167], v[98:99], off offset:288
	v_lshl_add_u64 v[166:167], v[166:167], 0, s[34:35]
	s_waitcnt vmcnt(31)
	v_lshlrev_b32_e32 v158, 16, v188
	v_and_b32_e32 v159, 0xffff0000, v188
	v_lshlrev_b32_e32 v160, 16, v189
	v_and_b32_e32 v161, 0xffff0000, v189
	v_pk_add_f32 v[94:95], v[94:95], v[158:159]
	v_pk_add_f32 v[96:97], v[96:97], v[160:161]
	v_cvt_pk_bf16_f32 v94, v94, v95
	v_cvt_pk_bf16_f32 v95, v96, v97
	global_store_dwordx2 v[166:167], v[94:95], off
	s_waitcnt vmcnt(31)
	v_lshlrev_b32_e32 v162, 16, v190
	v_and_b32_e32 v163, 0xffff0000, v190
	v_lshlrev_b32_e32 v164, 16, v191
	v_and_b32_e32 v165, 0xffff0000, v191
	v_pk_add_f32 v[90:91], v[90:91], v[162:163]
	v_pk_add_f32 v[92:93], v[92:93], v[164:165]
	v_cvt_pk_bf16_f32 v90, v90, v91
	v_cvt_pk_bf16_f32 v91, v92, v93
	global_store_dwordx2 v[166:167], v[90:91], off offset:32
	s_waitcnt vmcnt(31)
	v_lshlrev_b32_e32 v158, 16, v192
	v_and_b32_e32 v159, 0xffff0000, v192
	v_lshlrev_b32_e32 v160, 16, v193
	v_and_b32_e32 v161, 0xffff0000, v193
	v_pk_add_f32 v[86:87], v[86:87], v[158:159]
	v_pk_add_f32 v[88:89], v[88:89], v[160:161]
	v_cvt_pk_bf16_f32 v86, v86, v87
	v_cvt_pk_bf16_f32 v87, v88, v89
	global_store_dwordx2 v[166:167], v[86:87], off offset:256
	s_waitcnt vmcnt(31)
	v_lshlrev_b32_e32 v162, 16, v194
	v_and_b32_e32 v163, 0xffff0000, v194
	v_lshlrev_b32_e32 v164, 16, v195
	v_and_b32_e32 v165, 0xffff0000, v195
	v_pk_add_f32 v[82:83], v[82:83], v[162:163]
	v_pk_add_f32 v[84:85], v[84:85], v[164:165]
	v_cvt_pk_bf16_f32 v82, v82, v83
	v_cvt_pk_bf16_f32 v83, v84, v85
	global_store_dwordx2 v[166:167], v[82:83], off offset:288
	v_lshl_add_u64 v[166:167], v[166:167], 0, s[34:35]
	s_waitcnt vmcnt(31)
	v_lshlrev_b32_e32 v158, 16, v196
	v_and_b32_e32 v159, 0xffff0000, v196
	v_lshlrev_b32_e32 v160, 16, v197
	v_and_b32_e32 v161, 0xffff0000, v197
	v_pk_add_f32 v[78:79], v[78:79], v[158:159]
	v_pk_add_f32 v[80:81], v[80:81], v[160:161]
	v_cvt_pk_bf16_f32 v78, v78, v79
	v_cvt_pk_bf16_f32 v79, v80, v81
	global_store_dwordx2 v[166:167], v[78:79], off
	s_waitcnt vmcnt(31)
	v_lshlrev_b32_e32 v162, 16, v198
	v_and_b32_e32 v163, 0xffff0000, v198
	v_lshlrev_b32_e32 v164, 16, v199
	v_and_b32_e32 v165, 0xffff0000, v199
	v_pk_add_f32 v[74:75], v[74:75], v[162:163]
	v_pk_add_f32 v[76:77], v[76:77], v[164:165]
	v_cvt_pk_bf16_f32 v74, v74, v75
	v_cvt_pk_bf16_f32 v75, v76, v77
	global_store_dwordx2 v[166:167], v[74:75], off offset:32
	s_waitcnt vmcnt(31)
	v_lshlrev_b32_e32 v158, 16, v200
	v_and_b32_e32 v159, 0xffff0000, v200
	v_lshlrev_b32_e32 v160, 16, v201
	v_and_b32_e32 v161, 0xffff0000, v201
	v_pk_add_f32 v[70:71], v[70:71], v[158:159]
	v_pk_add_f32 v[72:73], v[72:73], v[160:161]
	v_cvt_pk_bf16_f32 v70, v70, v71
	v_cvt_pk_bf16_f32 v71, v72, v73
	global_store_dwordx2 v[166:167], v[70:71], off offset:256
	s_waitcnt vmcnt(31)
	v_lshlrev_b32_e32 v162, 16, v202
	v_and_b32_e32 v163, 0xffff0000, v202
	v_lshlrev_b32_e32 v164, 16, v203
	v_and_b32_e32 v165, 0xffff0000, v203
	v_pk_add_f32 v[66:67], v[66:67], v[162:163]
	v_pk_add_f32 v[68:69], v[68:69], v[164:165]
	v_cvt_pk_bf16_f32 v66, v66, v67
	v_cvt_pk_bf16_f32 v67, v68, v69
	global_store_dwordx2 v[166:167], v[66:67], off offset:288
	v_lshl_add_u64 v[166:167], v[166:167], 0, s[36:37]
	s_waitcnt vmcnt(31)
	v_lshlrev_b32_e32 v158, 16, v204
	v_and_b32_e32 v159, 0xffff0000, v204
	v_lshlrev_b32_e32 v160, 16, v205
	v_and_b32_e32 v161, 0xffff0000, v205
	v_pk_add_f32 v[62:63], v[62:63], v[158:159]
	v_pk_add_f32 v[64:65], v[64:65], v[160:161]
	v_cvt_pk_bf16_f32 v62, v62, v63
	v_cvt_pk_bf16_f32 v63, v64, v65
	global_store_dwordx2 v[166:167], v[62:63], off
	s_waitcnt vmcnt(31)
	v_lshlrev_b32_e32 v162, 16, v206
	v_and_b32_e32 v163, 0xffff0000, v206
	v_lshlrev_b32_e32 v164, 16, v207
	v_and_b32_e32 v165, 0xffff0000, v207
	v_pk_add_f32 v[58:59], v[58:59], v[162:163]
	v_pk_add_f32 v[60:61], v[60:61], v[164:165]
	v_cvt_pk_bf16_f32 v58, v58, v59
	v_cvt_pk_bf16_f32 v59, v60, v61
	global_store_dwordx2 v[166:167], v[58:59], off offset:32
	s_waitcnt vmcnt(31)
	v_lshlrev_b32_e32 v158, 16, v208
	v_and_b32_e32 v159, 0xffff0000, v208
	v_lshlrev_b32_e32 v160, 16, v209
	v_and_b32_e32 v161, 0xffff0000, v209
	v_pk_add_f32 v[54:55], v[54:55], v[158:159]
	v_pk_add_f32 v[56:57], v[56:57], v[160:161]
	v_cvt_pk_bf16_f32 v54, v54, v55
	v_cvt_pk_bf16_f32 v55, v56, v57
	global_store_dwordx2 v[166:167], v[54:55], off offset:256
	s_waitcnt vmcnt(31)
	v_lshlrev_b32_e32 v162, 16, v210
	v_and_b32_e32 v163, 0xffff0000, v210
	v_lshlrev_b32_e32 v164, 16, v211
	v_and_b32_e32 v165, 0xffff0000, v211
	v_pk_add_f32 v[50:51], v[50:51], v[162:163]
	v_pk_add_f32 v[52:53], v[52:53], v[164:165]
	v_cvt_pk_bf16_f32 v50, v50, v51
	v_cvt_pk_bf16_f32 v51, v52, v53
	global_store_dwordx2 v[166:167], v[50:51], off offset:288
	v_lshl_add_u64 v[166:167], v[166:167], 0, s[34:35]
	s_waitcnt vmcnt(31)
; DI unsigned pkbf(float lo, float hi) { typedef __bf16 b2 __attribute__((ext_vector_type(2))); typedef float f2 __attribute__((ext_vector_type(2))); const f2 v = {lo, hi}; return __builtin_bit_cast(unsigned, __builtin_convertvector(v, b2)); }
;     DI void operator()(const pg8::f32x4 (&acc)[2][2][4][2], const pg8::Unit& u, int wr, int wc, int fr, int fq) const {
;         const int row0 = u.pm * 256 + wr * 64 + fr, col0 = u.pn * 256 + wc * 32 + 4 * fq;
; #pragma unroll
;         for (int ai = 0; ai < 2; ++ai)
; #pragma unroll
;             for (int m = 0; m < 4; ++m) { const size_t off = (size_t)(row0 + ai * 128 + m * 16) * ldc + col0;
; #pragma unroll
;                 for (int bj = 0; bj < 2; ++bj)
; #pragma unroll
;                     for (int n = 0; n < 2; ++n) { pg8::f32x4 b;
;                         if constexpr (BASE_BF16) { const uint2 w = *(const uint2*)((const bf16*)base + off + bj * 128 + n * 16);
;                             b[0] = __uint_as_float(w.x << 16); b[1] = __uint_as_float(w.x & 0xffff0000u); b[2] = __uint_as_float(w.y << 16); b[3] = __uint_as_float(w.y & 0xffff0000u); }
;                         else b = *(const pg8::f32x4*)((const float*)base + off + bj * 128 + n * 16);
;                         b += acc[ai][bj][m][n]; uint2 o; o.x = pkbf(b[0], b[1]); o.y = pkbf(b[2], b[3]); *(uint2*)(out + off + bj * 128 + n * 16) = o; } }
	v_lshlrev_b32_e32 v158, 16, v212
	v_and_b32_e32 v159, 0xffff0000, v212
	v_lshlrev_b32_e32 v160, 16, v213
	v_and_b32_e32 v161, 0xffff0000, v213
	v_pk_add_f32 v[46:47], v[46:47], v[158:159]
	v_pk_add_f32 v[48:49], v[48:49], v[160:161]
	v_cvt_pk_bf16_f32 v46, v46, v47
	v_cvt_pk_bf16_f32 v47, v48, v49
	global_store_dwordx2 v[166:167], v[46:47], off
	s_waitcnt vmcnt(31)
	v_lshlrev_b32_e32 v162, 16, v214
	v_and_b32_e32 v163, 0xffff0000, v214
	v_lshlrev_b32_e32 v164, 16, v215
	v_and_b32_e32 v165, 0xffff0000, v215
	v_pk_add_f32 v[42:43], v[42:43], v[162:163]
	v_pk_add_f32 v[44:45], v[44:45], v[164:165]
	v_cvt_pk_bf16_f32 v42, v42, v43
	v_cvt_pk_bf16_f32 v43, v44, v45
	global_store_dwordx2 v[166:167], v[42:43], off offset:32
	s_waitcnt vmcnt(31)
	v_lshlrev_b32_e32 v158, 16, v216
	v_and_b32_e32 v159, 0xffff0000, v216
	v_lshlrev_b32_e32 v160, 16, v217
	v_and_b32_e32 v161, 0xffff0000, v217
	v_pk_add_f32 v[38:39], v[38:39], v[158:159]
	v_pk_add_f32 v[40:41], v[40:41], v[160:161]
	v_cvt_pk_bf16_f32 v38, v38, v39
	v_cvt_pk_bf16_f32 v39, v40, v41
	global_store_dwordx2 v[166:167], v[38:39], off offset:256
	s_waitcnt vmcnt(31)
	v_lshlrev_b32_e32 v162, 16, v218
	v_and_b32_e32 v163, 0xffff0000, v218
	v_lshlrev_b32_e32 v164, 16, v219
	v_and_b32_e32 v165, 0xffff0000, v219
	v_pk_add_f32 v[34:35], v[34:35], v[162:163]
	v_pk_add_f32 v[36:37], v[36:37], v[164:165]
	v_cvt_pk_bf16_f32 v34, v34, v35
	v_cvt_pk_bf16_f32 v35, v36, v37
	global_store_dwordx2 v[166:167], v[34:35], off offset:288
	v_lshl_add_u64 v[166:167], v[166:167], 0, s[34:35]
	s_waitcnt vmcnt(31)
	v_lshlrev_b32_e32 v158, 16, v220
	v_and_b32_e32 v159, 0xffff0000, v220
	v_lshlrev_b32_e32 v160, 16, v221
	v_and_b32_e32 v161, 0xffff0000, v221
	v_pk_add_f32 v[30:31], v[30:31], v[158:159]
	v_pk_add_f32 v[32:33], v[32:33], v[160:161]
	v_cvt_pk_bf16_f32 v30, v30, v31
	v_cvt_pk_bf16_f32 v31, v32, v33
	global_store_dwordx2 v[166:167], v[30:31], off
	s_waitcnt vmcnt(31)
	v_lshlrev_b32_e32 v162, 16, v222
	v_and_b32_e32 v163, 0xffff0000, v222
	v_lshlrev_b32_e32 v164, 16, v223
	v_and_b32_e32 v165, 0xffff0000, v223
	v_pk_add_f32 v[26:27], v[26:27], v[162:163]
	v_pk_add_f32 v[28:29], v[28:29], v[164:165]
	v_cvt_pk_bf16_f32 v26, v26, v27
	v_cvt_pk_bf16_f32 v27, v28, v29
	global_store_dwordx2 v[166:167], v[26:27], off offset:32
	s_waitcnt vmcnt(31)
	v_lshlrev_b32_e32 v158, 16, v224
	v_and_b32_e32 v159, 0xffff0000, v224
	v_lshlrev_b32_e32 v160, 16, v225
	v_and_b32_e32 v161, 0xffff0000, v225
	v_pk_add_f32 v[22:23], v[22:23], v[158:159]
	v_pk_add_f32 v[24:25], v[24:25], v[160:161]
	v_cvt_pk_bf16_f32 v22, v22, v23
	v_cvt_pk_bf16_f32 v23, v24, v25
	global_store_dwordx2 v[166:167], v[22:23], off offset:256
	s_waitcnt vmcnt(31)
	v_lshlrev_b32_e32 v162, 16, v226
	v_and_b32_e32 v163, 0xffff0000, v226
	v_lshlrev_b32_e32 v164, 16, v227
	v_and_b32_e32 v165, 0xffff0000, v227
	v_pk_add_f32 v[18:19], v[18:19], v[162:163]
	v_pk_add_f32 v[20:21], v[20:21], v[164:165]
	v_cvt_pk_bf16_f32 v18, v18, v19
	v_cvt_pk_bf16_f32 v19, v20, v21
	global_store_dwordx2 v[166:167], v[18:19], off offset:288
	v_lshl_add_u64 v[166:167], v[166:167], 0, s[34:35]
	s_waitcnt vmcnt(31)
	v_lshlrev_b32_e32 v158, 16, v228
	v_and_b32_e32 v159, 0xffff0000, v228
	v_lshlrev_b32_e32 v160, 16, v229
	v_and_b32_e32 v161, 0xffff0000, v229
	v_pk_add_f32 v[14:15], v[14:15], v[158:159]
	v_pk_add_f32 v[16:17], v[16:17], v[160:161]
	v_cvt_pk_bf16_f32 v14, v14, v15
	v_cvt_pk_bf16_f32 v15, v16, v17
	global_store_dwordx2 v[166:167], v[14:15], off
	s_waitcnt vmcnt(31)
	v_lshlrev_b32_e32 v162, 16, v230
	v_and_b32_e32 v163, 0xffff0000, v230
	v_lshlrev_b32_e32 v164, 16, v231
	v_and_b32_e32 v165, 0xffff0000, v231
	v_pk_add_f32 v[10:11], v[10:11], v[162:163]
	v_pk_add_f32 v[12:13], v[12:13], v[164:165]
	v_cvt_pk_bf16_f32 v10, v10, v11
	v_cvt_pk_bf16_f32 v11, v12, v13
	global_store_dwordx2 v[166:167], v[10:11], off offset:32
	s_waitcnt vmcnt(31)
	v_lshlrev_b32_e32 v158, 16, v236
	v_and_b32_e32 v159, 0xffff0000, v236
	v_lshlrev_b32_e32 v160, 16, v237
	v_and_b32_e32 v161, 0xffff0000, v237
	v_pk_add_f32 v[6:7], v[6:7], v[158:159]
	v_pk_add_f32 v[8:9], v[8:9], v[160:161]
	v_cvt_pk_bf16_f32 v6, v6, v7
	v_cvt_pk_bf16_f32 v7, v8, v9
	global_store_dwordx2 v[166:167], v[6:7], off offset:256
	s_waitcnt vmcnt(31)
	v_lshlrev_b32_e32 v162, 16, v238
	v_and_b32_e32 v163, 0xffff0000, v238
	v_lshlrev_b32_e32 v164, 16, v239
	v_and_b32_e32 v165, 0xffff0000, v239
	v_pk_add_f32 v[2:3], v[2:3], v[162:163]
	v_pk_add_f32 v[4:5], v[4:5], v[164:165]
	v_cvt_pk_bf16_f32 v2, v2, v3
	v_cvt_pk_bf16_f32 v3, v4, v5
	global_store_dwordx2 v[166:167], v[2:3], off offset:288
	s_andn2_b64 vcc, exec, s[0:1]
	s_mov_b64 s[0:1], -1
	s_cbranch_vccnz .LBB0_2562
	s_andn2_b64 vcc, exec, s[6:7]
	s_cbranch_vccnz .LBB0_2561
	s_barrier
	s_branch .LBB0_2561
